# v033 plus attention tile loop back-edge rotation: loop-carried moves ahead of the tile barrier, loop closes with one s_cbranch_scc0
# speedup vs baseline: 1.0110x; 1.0013x over previous
; #define SWRITE_B(b) do { LAS char* vb_ = V_lds + (b) * SHM_V2 + vst00; *(LAS bf16x8*)(vb_ + 16384) = sa0; *(LAS bf16x8*)(vb_ + 18432) = sa1; } while (0)
; __device__ __forceinline__ void finishSM(f32x16& p0, f32x16& p1, float alpha, float& l_reg, bf16x8& pa0, bf16x8& pa1, bf16x8& pa2, bf16x8& pa3) {
;     ...
;   l_reg = l_reg * alpha + ps;
; template <int LDQ, int LDK, int LDO>
; __device__ __forceinline__ void attn_body256(const bf16_t* __restrict__ Qb, const bf16_t* __restrict__ Kh, const bf16_t* __restrict__ Vh, float* __restrict__ Ob, int seq, LAS char* lds) {
;     ...
;     if (j + 1 < NT) { asm volatile("s_waitcnt vmcnt(0)" ::: "memory"); SWRITE_B((j + 1) & 1); }
;     __syncthreads();
;   }
.LBB0_944:
	s_add_u32 s82, s82, 0xc2000
	v_add_f32_e32 v132, v246, v247
	s_addc_u32 s83, s83, 0
	s_add_i32 s86, s86, 0x8000
	v_fmac_f32_e32 v132, v245, v220
	s_cmp_eq_u32 s82, 0x1840000
	s_mov_b32 s10, s87
	v_mov_b32_e32 v248, v2
	v_mov_b32_e32 v245, v132
	s_waitcnt lgkmcnt(0)
	s_barrier
	s_cbranch_scc0 .LBB0_934
